# M2 prologue: lambda parameter loads requested together; the two 64-lane sums by DPP reduction instead of 12 dependent ds_bpermute round trips
# baseline (speedup 1.0000x reference)
.LBB0_417:
	s_or_b64 exec, exec, s[6:7]
	s_waitcnt lgkmcnt(0)
	ds_read_b32 v2, v0 offset:592
	ds_read_b32 v3, v0 offset:596
	ds_read_b32 v8, v0 offset:600
	ds_read_b32 v9, v0 offset:604
	s_waitcnt lgkmcnt(3)
	v_readfirstlane_b32 s0, v2
	s_waitcnt lgkmcnt(2)
	v_readfirstlane_b32 s1, v3
	s_add_u32 s0, s0, s12
	v_lshlrev_b32_e32 v2, 2, v1
	s_addc_u32 s1, s1, s13
	v_and_b32_e32 v3, 0xfc, v2
	s_nop 0
	global_load_dword v1, v3, s[0:1]
	global_load_dword v4, v3, s[0:1] offset:256
	global_load_dword v10, v3, s[0:1] offset:512
	global_load_dword v11, v3, s[0:1] offset:768
	s_waitcnt vmcnt(2)
	v_mul_f32_e32 v5, v1, v4
	s_nop 1
	v_mov_b32_dpp v6, v5 quad_perm:[1,0,3,2] row_mask:0xf bank_mask:0xf
	s_nop 1
	v_fmac_f32_e32 v6, v1, v4
	s_nop 1
	v_add_f32_dpp v6, v6, v6 quad_perm:[2,3,0,1] row_mask:0xf bank_mask:0xf
	s_nop 1
	v_add_f32_dpp v6, v6, v6 row_half_mirror row_mask:0xf bank_mask:0xf
	s_nop 1
	v_add_f32_dpp v6, v6, v6 row_mirror row_mask:0xf bank_mask:0xf
	s_nop 1
	v_add_f32_dpp v6, v6, v6 row_bcast:15 row_mask:0xa bank_mask:0xf
	s_nop 1
	v_add_f32_dpp v6, v6, v6 row_bcast:31 row_mask:0xc bank_mask:0xf
	s_waitcnt vmcnt(0)
	v_mul_f32_e32 v5, v10, v11
	s_nop 1
	v_mov_b32_dpp v7, v5 quad_perm:[1,0,3,2] row_mask:0xf bank_mask:0xf
	s_nop 1
	v_fmac_f32_e32 v7, v10, v11
	s_nop 1
	v_add_f32_dpp v7, v7, v7 quad_perm:[2,3,0,1] row_mask:0xf bank_mask:0xf
	s_nop 1
	v_add_f32_dpp v7, v7, v7 row_half_mirror row_mask:0xf bank_mask:0xf
	s_nop 1
	v_add_f32_dpp v7, v7, v7 row_mirror row_mask:0xf bank_mask:0xf
	s_nop 1
	v_add_f32_dpp v7, v7, v7 row_bcast:15 row_mask:0xa bank_mask:0xf
	s_nop 1
	v_add_f32_dpp v7, v7, v7 row_bcast:31 row_mask:0xc bank_mask:0xf
	s_nop 0
	v_readlane_b32 s100, v6, 63
	v_readlane_b32 s101, v7, 63
	s_waitcnt lgkmcnt(0)
	v_readfirstlane_b32 s1, v9
	v_readfirstlane_b32 s0, v8
	s_cmp_ge_i32 s89, s86
	s_cbranch_scc1 .LBB0_394
	v_mov_b32_e32 v1, s100
	v_mov_b32_e32 v2, s101
	v_mul_f32_e32 v3, 0x3fb8aa3b, v1
	s_mov_b32 s4, 0x3fb8aa3b
	v_fma_f32 v4, v1, s4, -v3
	v_rndne_f32_e32 v5, v3
	v_fmac_f32_e32 v4, 0x32a5705f, v1
	v_sub_f32_e32 v3, v3, v5
	v_add_f32_e32 v3, v3, v4
	v_exp_f32_e32 v3, v3
	v_cvt_i32_f32_e32 v4, v5
	s_mov_b32 s5, 0xc2ce8ed0
	v_cmp_ngt_f32_e32 vcc, s5, v1
	s_mov_b32 s6, 0x42b17218
	v_ldexp_f32 v3, v3, v4
	v_cndmask_b32_e32 v3, 0, v3, vcc
	v_cmp_nlt_f32_e32 vcc, s6, v1
	s_nop 1
	v_cndmask_b32_e32 v1, v211, v3, vcc
	v_mul_f32_e32 v3, 0x3fb8aa3b, v2
	v_fma_f32 v4, v2, s4, -v3
	v_rndne_f32_e32 v5, v3
	v_fmac_f32_e32 v4, 0x32a5705f, v2
	v_sub_f32_e32 v3, v3, v5
	v_cmp_ngt_f32_e32 vcc, s5, v2
	v_readlane_b32 s4, v255, 21
	v_add_f32_e32 v3, v3, v4
	v_readlane_b32 s5, v255, 22
	s_add_u32 s0, s0, s4
	v_exp_f32_e32 v3, v3
	v_cvt_i32_f32_e32 v4, v5
	s_addc_u32 s1, s1, s5
	s_add_i32 s10, s90, 0
	s_add_u32 s80, s3, 0x11400000
	s_addc_u32 s81, s2, 0
	s_add_u32 s11, s3, 0x13800000
	v_ldexp_f32 v3, v3, v4
	s_addc_u32 s91, s2, 0
	v_cndmask_b32_e32 v3, 0, v3, vcc
	v_cmp_nlt_f32_e32 vcc, s6, v2
	s_add_u32 s82, s3, 0x28100000
	s_addc_u32 s83, s2, 0
	v_cndmask_b32_e32 v2, v211, v3, vcc
	s_add_i32 s92, s10, 0xf000
	v_sub_f32_e32 v1, v1, v2
	s_add_u32 s93, s3, 0x2c500000
	v_add_f32_e32 v206, v204, v1
	s_addc_u32 s94, s2, 0
	s_add_i32 s95, s10, 0x19000
	s_add_i32 s96, s10, 0x11000
	s_add_i32 s97, s10, 0x13000
	s_add_i32 s8, s10, 0x15000
	s_add_i32 s9, s10, 0x17000
	s_branch .LBB0_420
